# v64 + G1 tail last stage (row-tile totals added to the prefix, lane-permute, store): all 24 total rows read at once, adds under the same wave-uniform conditions, 28 store permutes together instead of
# speedup vs baseline: 1.0030x; 1.0030x over previous
; __device__ __forceinline__ unsigned pk2(float lo, float hi) { return pg8::cvt_pk_bf16(lo, hi); }
; #define MFMA16(a, b, c) __builtin_amdgcn_mfma_f32_16x16x32_bf16((a), (b), (c), 0, 0, 0)
; __device__ __forceinline__ float logsig16(float x) { return ((x < 0.f ? x : 0.f) - 0.6931471805599453f * __builtin_amdgcn_logf(1.0f + __builtin_amdgcn_exp2f(-1.4426950408889634f * fabsf(x)))) * (1.0f / 16.0f); }
; template <int layer> __device__ __forceinline__ void layer_phases(const Ctx& c, unsigned char* lds) {
;     ...
;                   {
;                     bf16x8 afr = (bf16x8){0, 0, 0, 0, 0, 0, 0, 0};
;                     if (g4 < 2) { const f32x4 x0 = *(const f32x4*)(glrl + (rt * 16 + ql) * 16 + 8 * g4), x1 = *(const f32x4*)(glrl + (rt * 16 + ql) * 16 + 8 * g4 + 4);
;                         v4u pa; pa.x = pk2(x0[0], x0[1]); pa.y = pk2(x0[2], x0[3]); pa.z = pk2(x1[0], x1[1]); pa.w = pk2(x1[2], x1[3]); afr = __builtin_bit_cast(bf16x8, pa); }
;                     f32x4 cv[8]; float* tot = (float*)(lds + 8192);
; #pragma unroll
;                     for (int ct = 0; ct < 8; ++ct) { const f32x4 z = MFMA16(wfr[ct], afr, ((f32x4){0.f, 0.f, 0.f, 0.f})) + bcl[ct];
;                         f32x4 v; v[0] = pg8::logsig16(z[0]); v[1] = pg8::logsig16(z[1]); v[2] = pg8::logsig16(z[2]); v[3] = pg8::logsig16(z[3]);
; #pragma unroll
;                         for (int st = 1; st < 16; st <<= 1) { f32x4 t;
; #pragma unroll
;                             for (int j = 0; j < 4; ++j) t[j] = __shfl_up(v[j], st, 16);
;                             if (ql >= st) v += t; }
;                         cv[ct] = v;
;                         if (ql == 15) *(f32x4*)(tot + rt * 256 + 16 * (8 * kh + ct) + 4 * g4) = v; }
.LBB0_269:
	s_or_b64 exec, exec, s[16:17]
	s_nop 0
	v_mfma_f32_16x16x32_bf16 v[66:69], v[2:5], v[70:73], 0
	v_and_b32_e32 v82, 0x70, v228
	v_add_u32_e32 v78, -1, v228
	v_cmp_lt_i32_e32 vcc, v78, v82
	s_nop 1
	v_cndmask_b32_e32 v78, v78, v228, vcc
	s_nop 1
	v_pk_add_f32 v[66:67], v[10:11], v[66:67]
	v_pk_add_f32 v[68:69], v[12:13], v[68:69]
	v_mul_f32_e64 v74, |v66|, s93
	v_mul_f32_e64 v75, |v67|, s93
	v_exp_f32_e32 v74, v74
	v_exp_f32_e32 v75, v75
	v_mul_f32_e64 v76, |v68|, s93
	v_mul_f32_e64 v77, |v69|, s93
	v_add_f32_e32 v74, 1.0, v74
	v_add_f32_e32 v75, 1.0, v75
	v_log_f32_e32 v74, v74
	v_log_f32_e32 v75, v75
	v_exp_f32_e32 v76, v76
	v_exp_f32_e32 v77, v77
	v_min_f32_e32 v67, 0, v67
	v_min_f32_e32 v66, 0, v66
	v_pk_fma_f32 v[66:67], v[74:75], s[64:65], v[66:67] op_sel_hi:[1,0,1] neg_lo:[1,0,0] neg_hi:[1,0,0]
	v_add_f32_e32 v74, 1.0, v76
	v_add_f32_e32 v75, 1.0, v77
	v_log_f32_e32 v74, v74
	v_log_f32_e32 v75, v75
	v_min_f32_e32 v69, 0, v69
	v_min_f32_e32 v68, 0, v68
	v_lshlrev_b32_e32 v98, 2, v78
	v_pk_fma_f32 v[68:69], v[74:75], s[64:65], v[68:69] op_sel_hi:[1,0,1] neg_lo:[1,0,0] neg_hi:[1,0,0]
	v_add_u32_e32 v74, -2, v228
	v_cmp_lt_i32_e32 vcc, v74, v82
	v_cndmask_b32_e32 v74, v74, v228, vcc
	v_lshlrev_b32_e32 v99, 2, v74
	v_add_u32_e32 v74, -4, v228
	v_cmp_lt_i32_e32 vcc, v74, v82
	v_cndmask_b32_e32 v74, v74, v228, vcc
	v_lshlrev_b32_e32 v100, 2, v74
	v_add_u32_e32 v74, -8, v228
	v_cmp_lt_i32_e32 vcc, v74, v82
	v_cndmask_b32_e32 v74, v74, v228, vcc
	v_lshlrev_b32_e32 v101, 2, v74
	v_pk_mul_f32 v[66:67], v[66:67], s[66:67] op_sel_hi:[1,0]
	v_pk_mul_f32 v[68:69], v[68:69], s[66:67] op_sel_hi:[1,0]
	s_nop 1
	v_add_f32_dpp v66, v66, v66 row_shr:1 row_mask:0xf bank_mask:0xf
	v_add_f32_dpp v67, v67, v67 row_shr:1 row_mask:0xf bank_mask:0xf
	v_add_f32_dpp v68, v68, v68 row_shr:1 row_mask:0xf bank_mask:0xf
	v_add_f32_dpp v69, v69, v69 row_shr:1 row_mask:0xf bank_mask:0xf
	v_add_f32_dpp v66, v66, v66 row_shr:2 row_mask:0xf bank_mask:0xf
	v_add_f32_dpp v67, v67, v67 row_shr:2 row_mask:0xf bank_mask:0xf
	v_add_f32_dpp v68, v68, v68 row_shr:2 row_mask:0xf bank_mask:0xf
	v_add_f32_dpp v69, v69, v69 row_shr:2 row_mask:0xf bank_mask:0xf
	v_add_f32_dpp v66, v66, v66 row_shr:4 row_mask:0xf bank_mask:0xf
	v_add_f32_dpp v67, v67, v67 row_shr:4 row_mask:0xf bank_mask:0xf
	v_add_f32_dpp v68, v68, v68 row_shr:4 row_mask:0xf bank_mask:0xf
	v_add_f32_dpp v69, v69, v69 row_shr:4 row_mask:0xf bank_mask:0xf
	v_add_f32_dpp v66, v66, v66 row_shr:8 row_mask:0xf bank_mask:0xf
	v_add_f32_dpp v67, v67, v67 row_shr:8 row_mask:0xf bank_mask:0xf
	v_add_f32_dpp v68, v68, v68 row_shr:8 row_mask:0xf bank_mask:0xf
	v_add_f32_dpp v69, v69, v69 row_shr:8 row_mask:0xf bank_mask:0xf
	s_and_saveexec_b64 s[16:17], s[6:7]
	v_add_u32_e32 v74, s3, v107
	ds_write_b128 v74, v[66:69] offset:8192
	s_or_b64 exec, exec, s[16:17]
	v_mfma_f32_16x16x32_bf16 v[74:77], v[6:9], v[70:73], 0
	s_nop 7
	v_pk_add_f32 v[74:75], v[14:15], v[74:75]
	v_pk_add_f32 v[76:77], v[16:17], v[76:77]
	v_mul_f32_e64 v78, |v74|, s93
	v_mul_f32_e64 v79, |v75|, s93
	v_exp_f32_e32 v78, v78
	v_exp_f32_e32 v79, v79
	v_mul_f32_e64 v80, |v76|, s93
	v_mul_f32_e64 v81, |v77|, s93
	v_add_f32_e32 v78, 1.0, v78
	v_add_f32_e32 v79, 1.0, v79
	v_log_f32_e32 v78, v78
	v_log_f32_e32 v79, v79
	v_exp_f32_e32 v80, v80
	v_exp_f32_e32 v81, v81
	v_min_f32_e32 v75, 0, v75
	v_min_f32_e32 v74, 0, v74
	v_pk_fma_f32 v[74:75], v[78:79], s[64:65], v[74:75] op_sel_hi:[1,0,1] neg_lo:[1,0,0] neg_hi:[1,0,0]
	v_add_f32_e32 v78, 1.0, v80
	v_add_f32_e32 v79, 1.0, v81
	v_log_f32_e32 v78, v78
	v_log_f32_e32 v79, v79
	v_min_f32_e32 v77, 0, v77
	v_min_f32_e32 v76, 0, v76
	v_pk_fma_f32 v[76:77], v[78:79], s[64:65], v[76:77] op_sel_hi:[1,0,1] neg_lo:[1,0,0] neg_hi:[1,0,0]
	v_pk_mul_f32 v[74:75], v[74:75], s[66:67] op_sel_hi:[1,0]
	v_pk_mul_f32 v[76:77], v[76:77], s[66:67] op_sel_hi:[1,0]
	s_nop 1
	v_add_f32_dpp v74, v74, v74 row_shr:1 row_mask:0xf bank_mask:0xf
	v_add_f32_dpp v75, v75, v75 row_shr:1 row_mask:0xf bank_mask:0xf
	v_add_f32_dpp v76, v76, v76 row_shr:1 row_mask:0xf bank_mask:0xf
	v_add_f32_dpp v77, v77, v77 row_shr:1 row_mask:0xf bank_mask:0xf
	v_add_f32_dpp v74, v74, v74 row_shr:2 row_mask:0xf bank_mask:0xf
	v_add_f32_dpp v75, v75, v75 row_shr:2 row_mask:0xf bank_mask:0xf
	v_add_f32_dpp v76, v76, v76 row_shr:2 row_mask:0xf bank_mask:0xf
	v_add_f32_dpp v77, v77, v77 row_shr:2 row_mask:0xf bank_mask:0xf
	v_add_f32_dpp v74, v74, v74 row_shr:4 row_mask:0xf bank_mask:0xf
	v_add_f32_dpp v75, v75, v75 row_shr:4 row_mask:0xf bank_mask:0xf
	v_add_f32_dpp v76, v76, v76 row_shr:4 row_mask:0xf bank_mask:0xf
	v_add_f32_dpp v77, v77, v77 row_shr:4 row_mask:0xf bank_mask:0xf
	v_add_f32_dpp v74, v74, v74 row_shr:8 row_mask:0xf bank_mask:0xf
	v_add_f32_dpp v75, v75, v75 row_shr:8 row_mask:0xf bank_mask:0xf
	v_add_f32_dpp v76, v76, v76 row_shr:8 row_mask:0xf bank_mask:0xf
	v_add_f32_dpp v77, v77, v77 row_shr:8 row_mask:0xf bank_mask:0xf
	s_and_saveexec_b64 s[16:17], s[6:7]
	v_add_u32_e32 v78, s80, v107
	ds_write_b128 v78, v[74:77] offset:8192
	s_or_b64 exec, exec, s[16:17]
	v_mfma_f32_16x16x32_bf16 v[78:81], v[18:21], v[70:73], 0
	s_nop 7
	v_pk_add_f32 v[78:79], v[26:27], v[78:79]
	v_pk_add_f32 v[80:81], v[28:29], v[80:81]
	v_mul_f32_e64 v82, |v78|, s93
	v_mul_f32_e64 v83, |v79|, s93
	v_exp_f32_e32 v82, v82
	v_exp_f32_e32 v83, v83
	v_mul_f32_e64 v84, |v80|, s93
	v_mul_f32_e64 v85, |v81|, s93
	v_add_f32_e32 v82, 1.0, v82
	v_add_f32_e32 v83, 1.0, v83
	v_log_f32_e32 v82, v82
	v_log_f32_e32 v83, v83
	v_exp_f32_e32 v84, v84
	v_exp_f32_e32 v85, v85
	v_min_f32_e32 v79, 0, v79
	v_min_f32_e32 v78, 0, v78
	v_pk_fma_f32 v[78:79], v[82:83], s[64:65], v[78:79] op_sel_hi:[1,0,1] neg_lo:[1,0,0] neg_hi:[1,0,0]
; #define MFMA16(a, b, c) __builtin_amdgcn_mfma_f32_16x16x32_bf16((a), (b), (c), 0, 0, 0)
; __device__ __forceinline__ float logsig16(float x) { return ((x < 0.f ? x : 0.f) - 0.6931471805599453f * __builtin_amdgcn_logf(1.0f + __builtin_amdgcn_exp2f(-1.4426950408889634f * fabsf(x)))) * (1.0f / 16.0f); }
; template <int layer> __device__ __forceinline__ void layer_phases(const Ctx& c, unsigned char* lds) {
;     ...
;                     for (int ct = 0; ct < 8; ++ct) { const f32x4 z = MFMA16(wfr[ct], afr, ((f32x4){0.f, 0.f, 0.f, 0.f})) + bcl[ct];
;                         f32x4 v; v[0] = pg8::logsig16(z[0]); v[1] = pg8::logsig16(z[1]); v[2] = pg8::logsig16(z[2]); v[3] = pg8::logsig16(z[3]);
; #pragma unroll
;                         for (int st = 1; st < 16; st <<= 1) { f32x4 t;
; #pragma unroll
;                             for (int j = 0; j < 4; ++j) t[j] = __shfl_up(v[j], st, 16);
;                             if (ql >= st) v += t; }
;                         cv[ct] = v;
;                         if (ql == 15) *(f32x4*)(tot + rt * 256 + 16 * (8 * kh + ct) + 4 * g4) = v; }
	v_add_f32_e32 v82, 1.0, v84
	v_add_f32_e32 v83, 1.0, v85
	v_log_f32_e32 v82, v82
	v_log_f32_e32 v83, v83
	v_min_f32_e32 v81, 0, v81
	v_min_f32_e32 v80, 0, v80
	v_pk_fma_f32 v[80:81], v[82:83], s[64:65], v[80:81] op_sel_hi:[1,0,1] neg_lo:[1,0,0] neg_hi:[1,0,0]
	v_pk_mul_f32 v[78:79], v[78:79], s[66:67] op_sel_hi:[1,0]
	v_pk_mul_f32 v[80:81], v[80:81], s[66:67] op_sel_hi:[1,0]
	s_nop 1
	v_add_f32_dpp v78, v78, v78 row_shr:1 row_mask:0xf bank_mask:0xf
	v_add_f32_dpp v79, v79, v79 row_shr:1 row_mask:0xf bank_mask:0xf
	v_add_f32_dpp v80, v80, v80 row_shr:1 row_mask:0xf bank_mask:0xf
	v_add_f32_dpp v81, v81, v81 row_shr:1 row_mask:0xf bank_mask:0xf
	v_add_f32_dpp v78, v78, v78 row_shr:2 row_mask:0xf bank_mask:0xf
	v_add_f32_dpp v79, v79, v79 row_shr:2 row_mask:0xf bank_mask:0xf
	v_add_f32_dpp v80, v80, v80 row_shr:2 row_mask:0xf bank_mask:0xf
	v_add_f32_dpp v81, v81, v81 row_shr:2 row_mask:0xf bank_mask:0xf
	v_add_f32_dpp v78, v78, v78 row_shr:4 row_mask:0xf bank_mask:0xf
	v_add_f32_dpp v79, v79, v79 row_shr:4 row_mask:0xf bank_mask:0xf
	v_add_f32_dpp v80, v80, v80 row_shr:4 row_mask:0xf bank_mask:0xf
	v_add_f32_dpp v81, v81, v81 row_shr:4 row_mask:0xf bank_mask:0xf
	v_add_f32_dpp v78, v78, v78 row_shr:8 row_mask:0xf bank_mask:0xf
	v_add_f32_dpp v79, v79, v79 row_shr:8 row_mask:0xf bank_mask:0xf
	v_add_f32_dpp v80, v80, v80 row_shr:8 row_mask:0xf bank_mask:0xf
	v_add_f32_dpp v81, v81, v81 row_shr:8 row_mask:0xf bank_mask:0xf
	s_and_saveexec_b64 s[16:17], s[6:7]
	v_add_u32_e32 v82, s81, v107
	ds_write_b128 v82, v[78:81] offset:8192
	s_or_b64 exec, exec, s[16:17]
	v_mfma_f32_16x16x32_bf16 v[82:85], v[22:25], v[70:73], 0
	s_nop 7
	v_pk_add_f32 v[82:83], v[30:31], v[82:83]
	v_pk_add_f32 v[84:85], v[32:33], v[84:85]
	v_mul_f32_e64 v86, |v82|, s93
	v_mul_f32_e64 v87, |v83|, s93
	v_exp_f32_e32 v86, v86
	v_exp_f32_e32 v87, v87
	v_mul_f32_e64 v88, |v84|, s93
	v_mul_f32_e64 v89, |v85|, s93
	v_add_f32_e32 v86, 1.0, v86
	v_add_f32_e32 v87, 1.0, v87
	v_log_f32_e32 v86, v86
	v_log_f32_e32 v87, v87
	v_exp_f32_e32 v88, v88
	v_exp_f32_e32 v89, v89
	v_min_f32_e32 v83, 0, v83
	v_min_f32_e32 v82, 0, v82
	v_pk_fma_f32 v[82:83], v[86:87], s[64:65], v[82:83] op_sel_hi:[1,0,1] neg_lo:[1,0,0] neg_hi:[1,0,0]
	v_add_f32_e32 v86, 1.0, v88
	v_add_f32_e32 v87, 1.0, v89
	v_log_f32_e32 v86, v86
	v_log_f32_e32 v87, v87
	v_min_f32_e32 v85, 0, v85
	v_min_f32_e32 v84, 0, v84
	v_pk_fma_f32 v[84:85], v[86:87], s[64:65], v[84:85] op_sel_hi:[1,0,1] neg_lo:[1,0,0] neg_hi:[1,0,0]
	v_pk_mul_f32 v[82:83], v[82:83], s[66:67] op_sel_hi:[1,0]
	v_pk_mul_f32 v[84:85], v[84:85], s[66:67] op_sel_hi:[1,0]
	s_nop 1
	v_add_f32_dpp v82, v82, v82 row_shr:1 row_mask:0xf bank_mask:0xf
	v_add_f32_dpp v83, v83, v83 row_shr:1 row_mask:0xf bank_mask:0xf
	v_add_f32_dpp v84, v84, v84 row_shr:1 row_mask:0xf bank_mask:0xf
	v_add_f32_dpp v85, v85, v85 row_shr:1 row_mask:0xf bank_mask:0xf
	v_add_f32_dpp v82, v82, v82 row_shr:2 row_mask:0xf bank_mask:0xf
	v_add_f32_dpp v83, v83, v83 row_shr:2 row_mask:0xf bank_mask:0xf
	v_add_f32_dpp v84, v84, v84 row_shr:2 row_mask:0xf bank_mask:0xf
	v_add_f32_dpp v85, v85, v85 row_shr:2 row_mask:0xf bank_mask:0xf
	v_add_f32_dpp v82, v82, v82 row_shr:4 row_mask:0xf bank_mask:0xf
	v_add_f32_dpp v83, v83, v83 row_shr:4 row_mask:0xf bank_mask:0xf
	v_add_f32_dpp v84, v84, v84 row_shr:4 row_mask:0xf bank_mask:0xf
	v_add_f32_dpp v85, v85, v85 row_shr:4 row_mask:0xf bank_mask:0xf
	v_add_f32_dpp v82, v82, v82 row_shr:8 row_mask:0xf bank_mask:0xf
	v_add_f32_dpp v83, v83, v83 row_shr:8 row_mask:0xf bank_mask:0xf
	v_add_f32_dpp v84, v84, v84 row_shr:8 row_mask:0xf bank_mask:0xf
	v_add_f32_dpp v85, v85, v85 row_shr:8 row_mask:0xf bank_mask:0xf
	s_and_saveexec_b64 s[16:17], s[6:7]
	v_add_u32_e32 v86, s82, v107
	ds_write_b128 v86, v[82:85] offset:8192
	s_or_b64 exec, exec, s[16:17]
	v_mfma_f32_16x16x32_bf16 v[86:89], v[34:37], v[70:73], 0
	s_nop 7
	v_pk_add_f32 v[86:87], v[42:43], v[86:87]
	v_pk_add_f32 v[88:89], v[44:45], v[88:89]
	v_mul_f32_e64 v90, |v86|, s93
	v_mul_f32_e64 v91, |v87|, s93
	v_exp_f32_e32 v90, v90
	v_exp_f32_e32 v91, v91
	v_mul_f32_e64 v92, |v88|, s93
	v_mul_f32_e64 v93, |v89|, s93
	v_add_f32_e32 v90, 1.0, v90
	v_add_f32_e32 v91, 1.0, v91
	v_log_f32_e32 v90, v90
	v_log_f32_e32 v91, v91
	v_exp_f32_e32 v92, v92
	v_exp_f32_e32 v93, v93
	v_min_f32_e32 v87, 0, v87
	v_min_f32_e32 v86, 0, v86
	v_pk_fma_f32 v[86:87], v[90:91], s[64:65], v[86:87] op_sel_hi:[1,0,1] neg_lo:[1,0,0] neg_hi:[1,0,0]
	v_add_f32_e32 v90, 1.0, v92
	v_add_f32_e32 v91, 1.0, v93
	v_log_f32_e32 v90, v90
	v_log_f32_e32 v91, v91
	v_min_f32_e32 v89, 0, v89
	v_min_f32_e32 v88, 0, v88
	v_pk_fma_f32 v[88:89], v[90:91], s[64:65], v[88:89] op_sel_hi:[1,0,1] neg_lo:[1,0,0] neg_hi:[1,0,0]
	v_pk_mul_f32 v[86:87], v[86:87], s[66:67] op_sel_hi:[1,0]
	v_pk_mul_f32 v[88:89], v[88:89], s[66:67] op_sel_hi:[1,0]
	s_nop 1
	v_add_f32_dpp v86, v86, v86 row_shr:1 row_mask:0xf bank_mask:0xf
	v_add_f32_dpp v87, v87, v87 row_shr:1 row_mask:0xf bank_mask:0xf
	v_add_f32_dpp v88, v88, v88 row_shr:1 row_mask:0xf bank_mask:0xf
	v_add_f32_dpp v89, v89, v89 row_shr:1 row_mask:0xf bank_mask:0xf
	v_add_f32_dpp v86, v86, v86 row_shr:2 row_mask:0xf bank_mask:0xf
	v_add_f32_dpp v87, v87, v87 row_shr:2 row_mask:0xf bank_mask:0xf
	v_add_f32_dpp v88, v88, v88 row_shr:2 row_mask:0xf bank_mask:0xf
	v_add_f32_dpp v89, v89, v89 row_shr:2 row_mask:0xf bank_mask:0xf
	v_add_f32_dpp v86, v86, v86 row_shr:4 row_mask:0xf bank_mask:0xf
	v_add_f32_dpp v87, v87, v87 row_shr:4 row_mask:0xf bank_mask:0xf
	v_add_f32_dpp v88, v88, v88 row_shr:4 row_mask:0xf bank_mask:0xf
	v_add_f32_dpp v89, v89, v89 row_shr:4 row_mask:0xf bank_mask:0xf
; #define MFMA16(a, b, c) __builtin_amdgcn_mfma_f32_16x16x32_bf16((a), (b), (c), 0, 0, 0)
; __device__ __forceinline__ float logsig16(float x) { return ((x < 0.f ? x : 0.f) - 0.6931471805599453f * __builtin_amdgcn_logf(1.0f + __builtin_amdgcn_exp2f(-1.4426950408889634f * fabsf(x)))) * (1.0f / 16.0f); }
; template <int layer> __device__ __forceinline__ void layer_phases(const Ctx& c, unsigned char* lds) {
;     ...
;                     for (int ct = 0; ct < 8; ++ct) { const f32x4 z = MFMA16(wfr[ct], afr, ((f32x4){0.f, 0.f, 0.f, 0.f})) + bcl[ct];
;                         f32x4 v; v[0] = pg8::logsig16(z[0]); v[1] = pg8::logsig16(z[1]); v[2] = pg8::logsig16(z[2]); v[3] = pg8::logsig16(z[3]);
; #pragma unroll
;                         for (int st = 1; st < 16; st <<= 1) { f32x4 t;
; #pragma unroll
;                             for (int j = 0; j < 4; ++j) t[j] = __shfl_up(v[j], st, 16);
;                             if (ql >= st) v += t; }
;                         cv[ct] = v;
;                         if (ql == 15) *(f32x4*)(tot + rt * 256 + 16 * (8 * kh + ct) + 4 * g4) = v; }
	v_add_f32_dpp v86, v86, v86 row_shr:8 row_mask:0xf bank_mask:0xf
	v_add_f32_dpp v87, v87, v87 row_shr:8 row_mask:0xf bank_mask:0xf
	v_add_f32_dpp v88, v88, v88 row_shr:8 row_mask:0xf bank_mask:0xf
	v_add_f32_dpp v89, v89, v89 row_shr:8 row_mask:0xf bank_mask:0xf
	s_and_saveexec_b64 s[16:17], s[6:7]
	v_add_u32_e32 v90, s83, v107
	ds_write_b128 v90, v[86:89] offset:8192
	s_or_b64 exec, exec, s[16:17]
	v_mfma_f32_16x16x32_bf16 v[90:93], v[38:41], v[70:73], 0
	s_nop 7
	v_pk_add_f32 v[90:91], v[46:47], v[90:91]
	v_pk_add_f32 v[92:93], v[48:49], v[92:93]
	v_mul_f32_e64 v94, |v90|, s93
	v_mul_f32_e64 v95, |v91|, s93
	v_exp_f32_e32 v94, v94
	v_exp_f32_e32 v95, v95
	v_mul_f32_e64 v96, |v92|, s93
	v_mul_f32_e64 v97, |v93|, s93
	v_add_f32_e32 v94, 1.0, v94
	v_add_f32_e32 v95, 1.0, v95
	v_log_f32_e32 v94, v94
	v_log_f32_e32 v95, v95
	v_exp_f32_e32 v96, v96
	v_exp_f32_e32 v97, v97
	v_min_f32_e32 v91, 0, v91
	v_min_f32_e32 v90, 0, v90
	v_pk_fma_f32 v[90:91], v[94:95], s[64:65], v[90:91] op_sel_hi:[1,0,1] neg_lo:[1,0,0] neg_hi:[1,0,0]
	v_add_f32_e32 v94, 1.0, v96
	v_add_f32_e32 v95, 1.0, v97
	v_log_f32_e32 v94, v94
	v_log_f32_e32 v95, v95
	v_min_f32_e32 v93, 0, v93
	v_min_f32_e32 v92, 0, v92
	v_pk_fma_f32 v[92:93], v[94:95], s[64:65], v[92:93] op_sel_hi:[1,0,1] neg_lo:[1,0,0] neg_hi:[1,0,0]
	v_pk_mul_f32 v[90:91], v[90:91], s[66:67] op_sel_hi:[1,0]
	v_pk_mul_f32 v[92:93], v[92:93], s[66:67] op_sel_hi:[1,0]
	s_nop 1
	v_add_f32_dpp v90, v90, v90 row_shr:1 row_mask:0xf bank_mask:0xf
	v_add_f32_dpp v91, v91, v91 row_shr:1 row_mask:0xf bank_mask:0xf
	v_add_f32_dpp v92, v92, v92 row_shr:1 row_mask:0xf bank_mask:0xf
	v_add_f32_dpp v93, v93, v93 row_shr:1 row_mask:0xf bank_mask:0xf
	v_add_f32_dpp v90, v90, v90 row_shr:2 row_mask:0xf bank_mask:0xf
	v_add_f32_dpp v91, v91, v91 row_shr:2 row_mask:0xf bank_mask:0xf
	v_add_f32_dpp v92, v92, v92 row_shr:2 row_mask:0xf bank_mask:0xf
	v_add_f32_dpp v93, v93, v93 row_shr:2 row_mask:0xf bank_mask:0xf
	v_add_f32_dpp v90, v90, v90 row_shr:4 row_mask:0xf bank_mask:0xf
	v_add_f32_dpp v91, v91, v91 row_shr:4 row_mask:0xf bank_mask:0xf
	v_add_f32_dpp v92, v92, v92 row_shr:4 row_mask:0xf bank_mask:0xf
	v_add_f32_dpp v93, v93, v93 row_shr:4 row_mask:0xf bank_mask:0xf
	v_add_f32_dpp v90, v90, v90 row_shr:8 row_mask:0xf bank_mask:0xf
	v_add_f32_dpp v91, v91, v91 row_shr:8 row_mask:0xf bank_mask:0xf
	v_add_f32_dpp v92, v92, v92 row_shr:8 row_mask:0xf bank_mask:0xf
	v_add_f32_dpp v93, v93, v93 row_shr:8 row_mask:0xf bank_mask:0xf
	s_and_saveexec_b64 s[16:17], s[6:7]
	v_add_u32_e32 v94, s84, v107
	ds_write_b128 v94, v[90:93] offset:8192
	s_or_b64 exec, exec, s[16:17]
	v_mfma_f32_16x16x32_bf16 v[94:97], v[50:53], v[70:73], 0
	s_nop 7
	v_pk_add_f32 v[94:95], v[58:59], v[94:95]
	v_pk_add_f32 v[96:97], v[60:61], v[96:97]
	v_mul_f32_e64 v102, |v94|, s93
	v_mul_f32_e64 v103, |v95|, s93
	v_exp_f32_e32 v102, v102
	v_exp_f32_e32 v103, v103
	v_mul_f32_e64 v104, |v96|, s93
	v_mul_f32_e64 v105, |v97|, s93
	v_add_f32_e32 v102, 1.0, v102
	v_add_f32_e32 v103, 1.0, v103
	v_log_f32_e32 v102, v102
	v_log_f32_e32 v103, v103
	v_exp_f32_e32 v104, v104
	v_exp_f32_e32 v105, v105
	v_min_f32_e32 v95, 0, v95
	v_min_f32_e32 v94, 0, v94
	v_pk_fma_f32 v[94:95], v[102:103], s[64:65], v[94:95] op_sel_hi:[1,0,1] neg_lo:[1,0,0] neg_hi:[1,0,0]
	v_add_f32_e32 v102, 1.0, v104
	v_add_f32_e32 v103, 1.0, v105
	v_log_f32_e32 v102, v102
	v_log_f32_e32 v103, v103
	v_min_f32_e32 v97, 0, v97
	v_min_f32_e32 v96, 0, v96
	v_pk_fma_f32 v[96:97], v[102:103], s[64:65], v[96:97] op_sel_hi:[1,0,1] neg_lo:[1,0,0] neg_hi:[1,0,0]
	v_pk_mul_f32 v[94:95], v[94:95], s[66:67] op_sel_hi:[1,0]
	v_pk_mul_f32 v[96:97], v[96:97], s[66:67] op_sel_hi:[1,0]
	s_nop 1
	v_add_f32_dpp v94, v94, v94 row_shr:1 row_mask:0xf bank_mask:0xf
	v_add_f32_dpp v95, v95, v95 row_shr:1 row_mask:0xf bank_mask:0xf
	v_add_f32_dpp v96, v96, v96 row_shr:1 row_mask:0xf bank_mask:0xf
	v_add_f32_dpp v97, v97, v97 row_shr:1 row_mask:0xf bank_mask:0xf
	v_add_f32_dpp v94, v94, v94 row_shr:2 row_mask:0xf bank_mask:0xf
	v_add_f32_dpp v95, v95, v95 row_shr:2 row_mask:0xf bank_mask:0xf
	v_add_f32_dpp v96, v96, v96 row_shr:2 row_mask:0xf bank_mask:0xf
	v_add_f32_dpp v97, v97, v97 row_shr:2 row_mask:0xf bank_mask:0xf
	v_add_f32_dpp v94, v94, v94 row_shr:4 row_mask:0xf bank_mask:0xf
	v_add_f32_dpp v95, v95, v95 row_shr:4 row_mask:0xf bank_mask:0xf
	v_add_f32_dpp v96, v96, v96 row_shr:4 row_mask:0xf bank_mask:0xf
	v_add_f32_dpp v97, v97, v97 row_shr:4 row_mask:0xf bank_mask:0xf
	v_add_f32_dpp v94, v94, v94 row_shr:8 row_mask:0xf bank_mask:0xf
	v_add_f32_dpp v95, v95, v95 row_shr:8 row_mask:0xf bank_mask:0xf
	v_add_f32_dpp v96, v96, v96 row_shr:8 row_mask:0xf bank_mask:0xf
	v_add_f32_dpp v97, v97, v97 row_shr:8 row_mask:0xf bank_mask:0xf
	s_and_saveexec_b64 s[16:17], s[6:7]
	v_add_u32_e32 v102, s85, v107
	ds_write_b128 v102, v[94:97] offset:8192
	s_or_b64 exec, exec, s[16:17]
	v_mfma_f32_16x16x32_bf16 v[70:73], v[54:57], v[70:73], 0
	s_nop 7
	v_pk_add_f32 v[70:71], v[62:63], v[70:71]
	v_pk_add_f32 v[72:73], v[64:65], v[72:73]
	v_mul_f32_e64 v102, |v70|, s93
	v_mul_f32_e64 v103, |v71|, s93
	v_exp_f32_e32 v102, v102
	v_exp_f32_e32 v103, v103
	v_mul_f32_e64 v104, |v72|, s93
	v_mul_f32_e64 v105, |v73|, s93
	v_add_f32_e32 v102, 1.0, v102
	v_add_f32_e32 v103, 1.0, v103
	v_log_f32_e32 v102, v102
	v_log_f32_e32 v103, v103
	v_exp_f32_e32 v104, v104
	v_exp_f32_e32 v105, v105
	v_min_f32_e32 v71, 0, v71
	v_min_f32_e32 v70, 0, v70
	v_pk_fma_f32 v[70:71], v[102:103], s[64:65], v[70:71] op_sel_hi:[1,0,1] neg_lo:[1,0,0] neg_hi:[1,0,0]
	v_add_f32_e32 v102, 1.0, v104
	v_add_f32_e32 v103, 1.0, v105
	v_log_f32_e32 v102, v102
	v_log_f32_e32 v103, v103
; template <int layer> __device__ __forceinline__ void layer_phases(const Ctx& c, unsigned char* lds) {
;     ...
;                     __syncthreads();
; #pragma unroll
;                     for (int ct = 0; ct < 8; ++ct) { f32x4 v = cv[ct];
; #pragma unroll
;                         for (int r2 = 0; r2 < 3; ++r2) if (r2 < rt) v += *(const f32x4*)(tot + r2 * 256 + 16 * (8 * kh + ct) + 4 * g4);
	v_min_f32_e32 v73, 0, v73
	v_min_f32_e32 v72, 0, v72
	v_pk_fma_f32 v[72:73], v[102:103], s[64:65], v[72:73] op_sel_hi:[1,0,1] neg_lo:[1,0,0] neg_hi:[1,0,0]
	v_pk_mul_f32 v[70:71], v[70:71], s[66:67] op_sel_hi:[1,0]
	v_pk_mul_f32 v[72:73], v[72:73], s[66:67] op_sel_hi:[1,0]
	s_nop 1
	v_add_f32_dpp v70, v70, v70 row_shr:1 row_mask:0xf bank_mask:0xf
	v_add_f32_dpp v71, v71, v71 row_shr:1 row_mask:0xf bank_mask:0xf
	v_add_f32_dpp v72, v72, v72 row_shr:1 row_mask:0xf bank_mask:0xf
	v_add_f32_dpp v73, v73, v73 row_shr:1 row_mask:0xf bank_mask:0xf
	v_add_f32_dpp v70, v70, v70 row_shr:2 row_mask:0xf bank_mask:0xf
	v_add_f32_dpp v71, v71, v71 row_shr:2 row_mask:0xf bank_mask:0xf
	v_add_f32_dpp v72, v72, v72 row_shr:2 row_mask:0xf bank_mask:0xf
	v_add_f32_dpp v73, v73, v73 row_shr:2 row_mask:0xf bank_mask:0xf
	v_add_f32_dpp v70, v70, v70 row_shr:4 row_mask:0xf bank_mask:0xf
	v_add_f32_dpp v71, v71, v71 row_shr:4 row_mask:0xf bank_mask:0xf
	v_add_f32_dpp v72, v72, v72 row_shr:4 row_mask:0xf bank_mask:0xf
	v_add_f32_dpp v73, v73, v73 row_shr:4 row_mask:0xf bank_mask:0xf
	v_add_f32_dpp v70, v70, v70 row_shr:8 row_mask:0xf bank_mask:0xf
	v_add_f32_dpp v71, v71, v71 row_shr:8 row_mask:0xf bank_mask:0xf
	v_add_f32_dpp v72, v72, v72 row_shr:8 row_mask:0xf bank_mask:0xf
	v_add_f32_dpp v73, v73, v73 row_shr:8 row_mask:0xf bank_mask:0xf
	s_and_saveexec_b64 s[16:17], s[6:7]
	v_add_u32_e32 v98, s88, v107
	ds_write_b128 v98, v[70:73] offset:8192
	s_or_b64 exec, exec, s[16:17]
	v_cndmask_b32_e64 v98, 0, 1, s[56:57]
	v_cmp_ne_u32_e64 s[16:17], 1, v98
	s_andn2_b64 vcc, exec, s[56:57]
	v_add_u32_e32 v98, s3, v144
	s_waitcnt lgkmcnt(0)
	s_barrier
	v_add_u32_e32 v250, s3, v144
	ds_read_b128 v[150:153], v250 offset:8192
	ds_read_b128 v[154:157], v250 offset:9216
	ds_read_b128 v[158:161], v250 offset:10240
	v_add_u32_e32 v251, s80, v144
	ds_read_b128 v[162:165], v251 offset:8192
	ds_read_b128 v[166:169], v251 offset:9216
	ds_read_b128 v[170:173], v251 offset:10240
	v_add_u32_e32 v250, s81, v144
	ds_read_b128 v[174:177], v250 offset:8192
	ds_read_b128 v[178:181], v250 offset:9216
	ds_read_b128 v[182:185], v250 offset:10240
	v_add_u32_e32 v251, s82, v144
	ds_read_b128 v[186:189], v251 offset:8192
	ds_read_b128 v[190:193], v251 offset:9216
	ds_read_b128 v[194:197], v251 offset:10240
	v_add_u32_e32 v250, s83, v144
	ds_read_b128 v[198:201], v250 offset:8192
	ds_read_b128 v[202:205], v250 offset:9216
	ds_read_b128 v[206:209], v250 offset:10240
	v_add_u32_e32 v251, s84, v144
	ds_read_b128 v[210:213], v251 offset:8192
	ds_read_b128 v[214:217], v251 offset:9216
	ds_read_b128 v[218:221], v251 offset:10240
	v_add_u32_e32 v250, s85, v144
	ds_read_b128 v[222:225], v250 offset:8192
	ds_read_b128 v[230:233], v250 offset:9216
	ds_read_b128 v[234:237], v250 offset:10240
	v_add_u32_e32 v251, s88, v144
	ds_read_b128 v[238:241], v251 offset:8192
	ds_read_b128 v[242:245], v251 offset:9216
	ds_read_b128 v[246:249], v251 offset:10240
	s_waitcnt lgkmcnt(0)
	s_andn2_b64 vcc, exec, s[56:57]
	s_cbranch_vccnz .Lla_skip0_0
	v_pk_add_f32 v[68:69], v[68:69], v[152:153]
	v_pk_add_f32 v[66:67], v[66:67], v[150:151]
	v_pk_add_f32 v[76:77], v[76:77], v[164:165]
	v_pk_add_f32 v[74:75], v[74:75], v[162:163]
	v_pk_add_f32 v[80:81], v[80:81], v[176:177]
	v_pk_add_f32 v[78:79], v[78:79], v[174:175]
	v_pk_add_f32 v[84:85], v[84:85], v[188:189]
	v_pk_add_f32 v[82:83], v[82:83], v[186:187]
	v_pk_add_f32 v[88:89], v[88:89], v[200:201]
	v_pk_add_f32 v[86:87], v[86:87], v[198:199]
	v_pk_add_f32 v[92:93], v[92:93], v[212:213]
	v_pk_add_f32 v[90:91], v[90:91], v[210:211]
	v_pk_add_f32 v[96:97], v[96:97], v[224:225]
	v_pk_add_f32 v[94:95], v[94:95], v[222:223]
	v_pk_add_f32 v[72:73], v[72:73], v[240:241]
	v_pk_add_f32 v[70:71], v[70:71], v[238:239]
; template <int layer> __device__ __forceinline__ void layer_phases(const Ctx& c, unsigned char* lds) {
;     ...
;                     __syncthreads();
; #pragma unroll
;                     for (int ct = 0; ct < 8; ++ct) { f32x4 v = cv[ct];
; #pragma unroll
;                         for (int r2 = 0; r2 < 3; ++r2) if (r2 < rt) v += *(const f32x4*)(tot + r2 * 256 + 16 * (8 * kh + ct) + 4 * g4);
;                         *(v4u*)(LA + (size_t)(blk * 64 + rt * 16 + (lane >> 2)) * 256 + 16 * (8 * kh + ct) + 4 * (lane & 3)) = lane_perm4(__builtin_bit_cast(v4u, v), QSRC_ST(lane)); } }
.Lla_skip0_0:
	s_andn2_b64 vcc, exec, s[58:59]
	s_cbranch_vccnz .Lla_skip0_1
	v_pk_add_f32 v[68:69], v[68:69], v[156:157]
	v_pk_add_f32 v[66:67], v[66:67], v[154:155]
	v_pk_add_f32 v[76:77], v[76:77], v[168:169]
	v_pk_add_f32 v[74:75], v[74:75], v[166:167]
	v_pk_add_f32 v[80:81], v[80:81], v[180:181]
	v_pk_add_f32 v[78:79], v[78:79], v[178:179]
	v_pk_add_f32 v[84:85], v[84:85], v[192:193]
	v_pk_add_f32 v[82:83], v[82:83], v[190:191]
	v_pk_add_f32 v[88:89], v[88:89], v[204:205]
	v_pk_add_f32 v[86:87], v[86:87], v[202:203]
	v_pk_add_f32 v[92:93], v[92:93], v[216:217]
	v_pk_add_f32 v[90:91], v[90:91], v[214:215]
	v_pk_add_f32 v[96:97], v[96:97], v[232:233]
	v_pk_add_f32 v[94:95], v[94:95], v[230:231]
	v_pk_add_f32 v[72:73], v[72:73], v[244:245]
	v_pk_add_f32 v[70:71], v[70:71], v[242:243]
.Lla_skip0_1:
	s_andn2_b64 vcc, exec, s[60:61]
	s_cbranch_vccnz .Lla_skip0_2
	v_pk_add_f32 v[68:69], v[68:69], v[160:161]
	v_pk_add_f32 v[66:67], v[66:67], v[158:159]
	v_pk_add_f32 v[76:77], v[76:77], v[172:173]
	v_pk_add_f32 v[74:75], v[74:75], v[170:171]
	v_pk_add_f32 v[80:81], v[80:81], v[184:185]
	v_pk_add_f32 v[78:79], v[78:79], v[182:183]
	v_pk_add_f32 v[84:85], v[84:85], v[196:197]
	v_pk_add_f32 v[82:83], v[82:83], v[194:195]
	v_pk_add_f32 v[88:89], v[88:89], v[208:209]
	v_pk_add_f32 v[86:87], v[86:87], v[206:207]
	v_pk_add_f32 v[92:93], v[92:93], v[220:221]
	v_pk_add_f32 v[90:91], v[90:91], v[218:219]
	v_pk_add_f32 v[96:97], v[96:97], v[236:237]
	v_pk_add_f32 v[94:95], v[94:95], v[234:235]
	v_pk_add_f32 v[72:73], v[72:73], v[248:249]
	v_pk_add_f32 v[70:71], v[70:71], v[246:247]
.Lla_skip0_2:
	ds_bpermute_b32 v150, v145, v66
	ds_bpermute_b32 v151, v145, v67
	ds_bpermute_b32 v152, v145, v68
	ds_bpermute_b32 v153, v145, v69
	ds_bpermute_b32 v154, v145, v74
	ds_bpermute_b32 v155, v145, v75
	ds_bpermute_b32 v156, v145, v76
	ds_bpermute_b32 v157, v145, v77
	ds_bpermute_b32 v158, v145, v78
	ds_bpermute_b32 v159, v145, v79
	ds_bpermute_b32 v160, v145, v80
	ds_bpermute_b32 v161, v145, v81
	ds_bpermute_b32 v162, v145, v82
	ds_bpermute_b32 v163, v145, v83
	ds_bpermute_b32 v164, v145, v84
	ds_bpermute_b32 v165, v145, v85
	ds_bpermute_b32 v166, v145, v86
	ds_bpermute_b32 v167, v145, v87
	ds_bpermute_b32 v168, v145, v88
	ds_bpermute_b32 v169, v145, v89
	ds_bpermute_b32 v170, v145, v90
	ds_bpermute_b32 v171, v145, v91
	ds_bpermute_b32 v172, v145, v92
	ds_bpermute_b32 v173, v145, v93
	ds_bpermute_b32 v174, v145, v94
	ds_bpermute_b32 v175, v145, v95
	ds_bpermute_b32 v176, v145, v96
	ds_bpermute_b32 v177, v145, v97
	v_lshlrev_b64 v[66:67], 10, v[142:143]
	v_lshl_add_u64 v[66:67], v[116:117], 0, v[66:67]
	s_waitcnt lgkmcnt(0)
	v_lshl_add_u64 v[68:69], s[22:23], 2, v[66:67]
	global_store_dwordx4 v[68:69], v[150:153], off
	v_lshl_add_u64 v[68:69], s[24:25], 2, v[66:67]
	global_store_dwordx4 v[68:69], v[154:157], off
	v_lshl_add_u64 v[68:69], s[26:27], 2, v[66:67]
	global_store_dwordx4 v[68:69], v[158:161], off
	v_lshl_add_u64 v[68:69], s[28:29], 2, v[66:67]
	global_store_dwordx4 v[68:69], v[162:165], off
	v_lshl_add_u64 v[68:69], s[30:31], 2, v[66:67]
	global_store_dwordx4 v[68:69], v[166:169], off
	v_lshl_add_u64 v[68:69], s[34:35], 2, v[66:67]
	global_store_dwordx4 v[68:69], v[170:173], off
	v_lshl_add_u64 v[68:69], s[36:37], 2, v[66:67]
	global_store_dwordx4 v[68:69], v[174:177], off
	s_branch .LBB0_262

; __device__ __forceinline__ float logsig16(float x) { return ((x < 0.f ? x : 0.f) - 0.6931471805599453f * __builtin_amdgcn_logf(1.0f + __builtin_amdgcn_exp2f(-1.4426950408889634f * fabsf(x)))) * (1.0f / 16.0f); }
; #define MFMA16(a, b, c) __builtin_amdgcn_mfma_f32_16x16x32_bf16((a), (b), (c), 0, 0, 0)
; template <int layer> __device__ __forceinline__ void layer_phases(const Ctx& c, unsigned char* lds) {
;     ...
;                     for (int ct = 0; ct < 8; ++ct) { const f32x4 z = MFMA16(wfr[ct], afr, ((f32x4){0.f, 0.f, 0.f, 0.f})) + bcl[ct];
;                         f32x4 v; v[0] = pg8::logsig16(z[0]); v[1] = pg8::logsig16(z[1]); v[2] = pg8::logsig16(z[2]); v[3] = pg8::logsig16(z[3]);
; #pragma unroll
;                         for (int st = 1; st < 16; st <<= 1) { f32x4 t;
; #pragma unroll
;                             for (int j = 0; j < 4; ++j) t[j] = __shfl_up(v[j], st, 16);
;                             if (ql >= st) v += t; }
;                         cv[ct] = v;
;                         if (ql == 15) *(f32x4*)(tot + rt * 256 + 16 * (8 * kh + ct) + 4 * g4) = v; }
.LBB0_960:
	s_or_b64 exec, exec, s[16:17]
	s_nop 0
	v_mfma_f32_16x16x32_bf16 v[66:69], v[2:5], v[70:73], 0
	v_and_b32_e32 v82, 0x70, v228
	v_add_u32_e32 v78, -1, v228
	v_cmp_lt_i32_e32 vcc, v78, v82
	s_nop 1
	v_cndmask_b32_e32 v78, v78, v228, vcc
	s_nop 1
	v_pk_add_f32 v[66:67], v[10:11], v[66:67]
	v_pk_add_f32 v[68:69], v[12:13], v[68:69]
	v_mul_f32_e64 v74, |v66|, s84
	v_mul_f32_e64 v75, |v67|, s84
	v_exp_f32_e32 v74, v74
	v_exp_f32_e32 v75, v75
	v_mul_f32_e64 v76, |v68|, s84
	v_mul_f32_e64 v77, |v69|, s84
	v_add_f32_e32 v74, 1.0, v74
	v_add_f32_e32 v75, 1.0, v75
	v_log_f32_e32 v74, v74
	v_log_f32_e32 v75, v75
	v_exp_f32_e32 v76, v76
	v_exp_f32_e32 v77, v77
	v_min_f32_e32 v67, 0, v67
	v_min_f32_e32 v66, 0, v66
	v_pk_fma_f32 v[66:67], v[74:75], s[66:67], v[66:67] op_sel_hi:[1,0,1] neg_lo:[1,0,0] neg_hi:[1,0,0]
	v_add_f32_e32 v74, 1.0, v76
	v_add_f32_e32 v75, 1.0, v77
	v_log_f32_e32 v74, v74
	v_log_f32_e32 v75, v75
	v_min_f32_e32 v69, 0, v69
	v_min_f32_e32 v68, 0, v68
	v_lshlrev_b32_e32 v98, 2, v78
	v_pk_fma_f32 v[68:69], v[74:75], s[66:67], v[68:69] op_sel_hi:[1,0,1] neg_lo:[1,0,0] neg_hi:[1,0,0]
	v_add_u32_e32 v74, -2, v228
	v_cmp_lt_i32_e32 vcc, v74, v82
	v_cndmask_b32_e32 v74, v74, v228, vcc
	v_lshlrev_b32_e32 v99, 2, v74
	v_add_u32_e32 v74, -4, v228
	v_cmp_lt_i32_e32 vcc, v74, v82
	v_cndmask_b32_e32 v74, v74, v228, vcc
	v_lshlrev_b32_e32 v100, 2, v74
	v_add_u32_e32 v74, -8, v228
	v_cmp_lt_i32_e32 vcc, v74, v82
	v_cndmask_b32_e32 v74, v74, v228, vcc
	v_lshlrev_b32_e32 v101, 2, v74
	v_pk_mul_f32 v[66:67], v[66:67], s[68:69] op_sel_hi:[1,0]
	v_pk_mul_f32 v[68:69], v[68:69], s[68:69] op_sel_hi:[1,0]
	s_nop 1
	v_add_f32_dpp v66, v66, v66 row_shr:1 row_mask:0xf bank_mask:0xf
	v_add_f32_dpp v67, v67, v67 row_shr:1 row_mask:0xf bank_mask:0xf
	v_add_f32_dpp v68, v68, v68 row_shr:1 row_mask:0xf bank_mask:0xf
	v_add_f32_dpp v69, v69, v69 row_shr:1 row_mask:0xf bank_mask:0xf
	v_add_f32_dpp v66, v66, v66 row_shr:2 row_mask:0xf bank_mask:0xf
	v_add_f32_dpp v67, v67, v67 row_shr:2 row_mask:0xf bank_mask:0xf
	v_add_f32_dpp v68, v68, v68 row_shr:2 row_mask:0xf bank_mask:0xf
	v_add_f32_dpp v69, v69, v69 row_shr:2 row_mask:0xf bank_mask:0xf
	v_add_f32_dpp v66, v66, v66 row_shr:4 row_mask:0xf bank_mask:0xf
	v_add_f32_dpp v67, v67, v67 row_shr:4 row_mask:0xf bank_mask:0xf
	v_add_f32_dpp v68, v68, v68 row_shr:4 row_mask:0xf bank_mask:0xf
	v_add_f32_dpp v69, v69, v69 row_shr:4 row_mask:0xf bank_mask:0xf
	v_add_f32_dpp v66, v66, v66 row_shr:8 row_mask:0xf bank_mask:0xf
	v_add_f32_dpp v67, v67, v67 row_shr:8 row_mask:0xf bank_mask:0xf
	v_add_f32_dpp v68, v68, v68 row_shr:8 row_mask:0xf bank_mask:0xf
	v_add_f32_dpp v69, v69, v69 row_shr:8 row_mask:0xf bank_mask:0xf
	s_and_saveexec_b64 s[16:17], s[6:7]
	v_add_u32_e32 v74, s3, v107
	ds_write_b128 v74, v[66:69] offset:8192
	s_or_b64 exec, exec, s[16:17]
	v_mfma_f32_16x16x32_bf16 v[74:77], v[6:9], v[70:73], 0
	s_nop 7
	v_pk_add_f32 v[74:75], v[14:15], v[74:75]
	v_pk_add_f32 v[76:77], v[16:17], v[76:77]
	v_mul_f32_e64 v78, |v74|, s84
	v_mul_f32_e64 v79, |v75|, s84
	v_exp_f32_e32 v78, v78
	v_exp_f32_e32 v79, v79
	v_mul_f32_e64 v80, |v76|, s84
	v_mul_f32_e64 v81, |v77|, s84
	v_add_f32_e32 v78, 1.0, v78
	v_add_f32_e32 v79, 1.0, v79
	v_log_f32_e32 v78, v78
	v_log_f32_e32 v79, v79
	v_exp_f32_e32 v80, v80
	v_exp_f32_e32 v81, v81
	v_min_f32_e32 v75, 0, v75
	v_min_f32_e32 v74, 0, v74
	v_pk_fma_f32 v[74:75], v[78:79], s[66:67], v[74:75] op_sel_hi:[1,0,1] neg_lo:[1,0,0] neg_hi:[1,0,0]
	v_add_f32_e32 v78, 1.0, v80
	v_add_f32_e32 v79, 1.0, v81
	v_log_f32_e32 v78, v78
	v_log_f32_e32 v79, v79
	v_min_f32_e32 v77, 0, v77
	v_min_f32_e32 v76, 0, v76
	v_pk_fma_f32 v[76:77], v[78:79], s[66:67], v[76:77] op_sel_hi:[1,0,1] neg_lo:[1,0,0] neg_hi:[1,0,0]
	v_pk_mul_f32 v[74:75], v[74:75], s[68:69] op_sel_hi:[1,0]
	v_pk_mul_f32 v[76:77], v[76:77], s[68:69] op_sel_hi:[1,0]
	s_nop 1
	v_add_f32_dpp v74, v74, v74 row_shr:1 row_mask:0xf bank_mask:0xf
	v_add_f32_dpp v75, v75, v75 row_shr:1 row_mask:0xf bank_mask:0xf
	v_add_f32_dpp v76, v76, v76 row_shr:1 row_mask:0xf bank_mask:0xf
	v_add_f32_dpp v77, v77, v77 row_shr:1 row_mask:0xf bank_mask:0xf
	v_add_f32_dpp v74, v74, v74 row_shr:2 row_mask:0xf bank_mask:0xf
	v_add_f32_dpp v75, v75, v75 row_shr:2 row_mask:0xf bank_mask:0xf
	v_add_f32_dpp v76, v76, v76 row_shr:2 row_mask:0xf bank_mask:0xf
	v_add_f32_dpp v77, v77, v77 row_shr:2 row_mask:0xf bank_mask:0xf
	v_add_f32_dpp v74, v74, v74 row_shr:4 row_mask:0xf bank_mask:0xf
	v_add_f32_dpp v75, v75, v75 row_shr:4 row_mask:0xf bank_mask:0xf
	v_add_f32_dpp v76, v76, v76 row_shr:4 row_mask:0xf bank_mask:0xf
	v_add_f32_dpp v77, v77, v77 row_shr:4 row_mask:0xf bank_mask:0xf
	v_add_f32_dpp v74, v74, v74 row_shr:8 row_mask:0xf bank_mask:0xf
	v_add_f32_dpp v75, v75, v75 row_shr:8 row_mask:0xf bank_mask:0xf
	v_add_f32_dpp v76, v76, v76 row_shr:8 row_mask:0xf bank_mask:0xf
	v_add_f32_dpp v77, v77, v77 row_shr:8 row_mask:0xf bank_mask:0xf
	s_and_saveexec_b64 s[16:17], s[6:7]
	v_add_u32_e32 v78, s56, v107
	ds_write_b128 v78, v[74:77] offset:8192
	s_or_b64 exec, exec, s[16:17]
	v_mfma_f32_16x16x32_bf16 v[78:81], v[18:21], v[70:73], 0
	s_nop 7
	v_pk_add_f32 v[78:79], v[26:27], v[78:79]
	v_pk_add_f32 v[80:81], v[28:29], v[80:81]
	v_mul_f32_e64 v82, |v78|, s84
	v_mul_f32_e64 v83, |v79|, s84
	v_exp_f32_e32 v82, v82
	v_exp_f32_e32 v83, v83
	v_mul_f32_e64 v84, |v80|, s84
	v_mul_f32_e64 v85, |v81|, s84
	v_add_f32_e32 v82, 1.0, v82
	v_add_f32_e32 v83, 1.0, v83
	v_log_f32_e32 v82, v82
	v_log_f32_e32 v83, v83
	v_exp_f32_e32 v84, v84
	v_exp_f32_e32 v85, v85
	v_min_f32_e32 v79, 0, v79
	v_min_f32_e32 v78, 0, v78
	v_pk_fma_f32 v[78:79], v[82:83], s[66:67], v[78:79] op_sel_hi:[1,0,1] neg_lo:[1,0,0] neg_hi:[1,0,0]
; __device__ __forceinline__ float logsig16(float x) { return ((x < 0.f ? x : 0.f) - 0.6931471805599453f * __builtin_amdgcn_logf(1.0f + __builtin_amdgcn_exp2f(-1.4426950408889634f * fabsf(x)))) * (1.0f / 16.0f); }
; #define MFMA16(a, b, c) __builtin_amdgcn_mfma_f32_16x16x32_bf16((a), (b), (c), 0, 0, 0)
; template <int layer> __device__ __forceinline__ void layer_phases(const Ctx& c, unsigned char* lds) {
;     ...
;                     for (int ct = 0; ct < 8; ++ct) { const f32x4 z = MFMA16(wfr[ct], afr, ((f32x4){0.f, 0.f, 0.f, 0.f})) + bcl[ct];
;                         f32x4 v; v[0] = pg8::logsig16(z[0]); v[1] = pg8::logsig16(z[1]); v[2] = pg8::logsig16(z[2]); v[3] = pg8::logsig16(z[3]);
; #pragma unroll
;                         for (int st = 1; st < 16; st <<= 1) { f32x4 t;
; #pragma unroll
;                             for (int j = 0; j < 4; ++j) t[j] = __shfl_up(v[j], st, 16);
;                             if (ql >= st) v += t; }
;                         cv[ct] = v;
;                         if (ql == 15) *(f32x4*)(tot + rt * 256 + 16 * (8 * kh + ct) + 4 * g4) = v; }
	v_add_f32_e32 v82, 1.0, v84
	v_add_f32_e32 v83, 1.0, v85
	v_log_f32_e32 v82, v82
	v_log_f32_e32 v83, v83
	v_min_f32_e32 v81, 0, v81
	v_min_f32_e32 v80, 0, v80
	v_pk_fma_f32 v[80:81], v[82:83], s[66:67], v[80:81] op_sel_hi:[1,0,1] neg_lo:[1,0,0] neg_hi:[1,0,0]
	v_pk_mul_f32 v[78:79], v[78:79], s[68:69] op_sel_hi:[1,0]
	v_pk_mul_f32 v[80:81], v[80:81], s[68:69] op_sel_hi:[1,0]
	s_nop 1
	v_add_f32_dpp v78, v78, v78 row_shr:1 row_mask:0xf bank_mask:0xf
	v_add_f32_dpp v79, v79, v79 row_shr:1 row_mask:0xf bank_mask:0xf
	v_add_f32_dpp v80, v80, v80 row_shr:1 row_mask:0xf bank_mask:0xf
	v_add_f32_dpp v81, v81, v81 row_shr:1 row_mask:0xf bank_mask:0xf
	v_add_f32_dpp v78, v78, v78 row_shr:2 row_mask:0xf bank_mask:0xf
	v_add_f32_dpp v79, v79, v79 row_shr:2 row_mask:0xf bank_mask:0xf
	v_add_f32_dpp v80, v80, v80 row_shr:2 row_mask:0xf bank_mask:0xf
	v_add_f32_dpp v81, v81, v81 row_shr:2 row_mask:0xf bank_mask:0xf
	v_add_f32_dpp v78, v78, v78 row_shr:4 row_mask:0xf bank_mask:0xf
	v_add_f32_dpp v79, v79, v79 row_shr:4 row_mask:0xf bank_mask:0xf
	v_add_f32_dpp v80, v80, v80 row_shr:4 row_mask:0xf bank_mask:0xf
	v_add_f32_dpp v81, v81, v81 row_shr:4 row_mask:0xf bank_mask:0xf
	v_add_f32_dpp v78, v78, v78 row_shr:8 row_mask:0xf bank_mask:0xf
	v_add_f32_dpp v79, v79, v79 row_shr:8 row_mask:0xf bank_mask:0xf
	v_add_f32_dpp v80, v80, v80 row_shr:8 row_mask:0xf bank_mask:0xf
	v_add_f32_dpp v81, v81, v81 row_shr:8 row_mask:0xf bank_mask:0xf
	s_and_saveexec_b64 s[16:17], s[6:7]
	v_add_u32_e32 v82, s57, v107
	ds_write_b128 v82, v[78:81] offset:8192
	s_or_b64 exec, exec, s[16:17]
	v_mfma_f32_16x16x32_bf16 v[82:85], v[22:25], v[70:73], 0
	s_nop 7
	v_pk_add_f32 v[82:83], v[30:31], v[82:83]
	v_pk_add_f32 v[84:85], v[32:33], v[84:85]
	v_mul_f32_e64 v86, |v82|, s84
	v_mul_f32_e64 v87, |v83|, s84
	v_exp_f32_e32 v86, v86
	v_exp_f32_e32 v87, v87
	v_mul_f32_e64 v88, |v84|, s84
	v_mul_f32_e64 v89, |v85|, s84
	v_add_f32_e32 v86, 1.0, v86
	v_add_f32_e32 v87, 1.0, v87
	v_log_f32_e32 v86, v86
	v_log_f32_e32 v87, v87
	v_exp_f32_e32 v88, v88
	v_exp_f32_e32 v89, v89
	v_min_f32_e32 v83, 0, v83
	v_min_f32_e32 v82, 0, v82
	v_pk_fma_f32 v[82:83], v[86:87], s[66:67], v[82:83] op_sel_hi:[1,0,1] neg_lo:[1,0,0] neg_hi:[1,0,0]
	v_add_f32_e32 v86, 1.0, v88
	v_add_f32_e32 v87, 1.0, v89
	v_log_f32_e32 v86, v86
	v_log_f32_e32 v87, v87
	v_min_f32_e32 v85, 0, v85
	v_min_f32_e32 v84, 0, v84
	v_pk_fma_f32 v[84:85], v[86:87], s[66:67], v[84:85] op_sel_hi:[1,0,1] neg_lo:[1,0,0] neg_hi:[1,0,0]
	v_pk_mul_f32 v[82:83], v[82:83], s[68:69] op_sel_hi:[1,0]
	v_pk_mul_f32 v[84:85], v[84:85], s[68:69] op_sel_hi:[1,0]
	s_nop 1
	v_add_f32_dpp v82, v82, v82 row_shr:1 row_mask:0xf bank_mask:0xf
	v_add_f32_dpp v83, v83, v83 row_shr:1 row_mask:0xf bank_mask:0xf
	v_add_f32_dpp v84, v84, v84 row_shr:1 row_mask:0xf bank_mask:0xf
	v_add_f32_dpp v85, v85, v85 row_shr:1 row_mask:0xf bank_mask:0xf
	v_add_f32_dpp v82, v82, v82 row_shr:2 row_mask:0xf bank_mask:0xf
	v_add_f32_dpp v83, v83, v83 row_shr:2 row_mask:0xf bank_mask:0xf
	v_add_f32_dpp v84, v84, v84 row_shr:2 row_mask:0xf bank_mask:0xf
	v_add_f32_dpp v85, v85, v85 row_shr:2 row_mask:0xf bank_mask:0xf
	v_add_f32_dpp v82, v82, v82 row_shr:4 row_mask:0xf bank_mask:0xf
	v_add_f32_dpp v83, v83, v83 row_shr:4 row_mask:0xf bank_mask:0xf
	v_add_f32_dpp v84, v84, v84 row_shr:4 row_mask:0xf bank_mask:0xf
	v_add_f32_dpp v85, v85, v85 row_shr:4 row_mask:0xf bank_mask:0xf
	v_add_f32_dpp v82, v82, v82 row_shr:8 row_mask:0xf bank_mask:0xf
	v_add_f32_dpp v83, v83, v83 row_shr:8 row_mask:0xf bank_mask:0xf
	v_add_f32_dpp v84, v84, v84 row_shr:8 row_mask:0xf bank_mask:0xf
	v_add_f32_dpp v85, v85, v85 row_shr:8 row_mask:0xf bank_mask:0xf
	s_and_saveexec_b64 s[16:17], s[6:7]
	v_add_u32_e32 v86, s67, v107
	ds_write_b128 v86, v[82:85] offset:8192
	s_or_b64 exec, exec, s[16:17]
	v_mfma_f32_16x16x32_bf16 v[86:89], v[34:37], v[70:73], 0
	s_nop 7
	v_pk_add_f32 v[86:87], v[42:43], v[86:87]
	v_pk_add_f32 v[88:89], v[44:45], v[88:89]
	v_mul_f32_e64 v90, |v86|, s84
	v_mul_f32_e64 v91, |v87|, s84
	v_exp_f32_e32 v90, v90
	v_exp_f32_e32 v91, v91
	v_mul_f32_e64 v92, |v88|, s84
	v_mul_f32_e64 v93, |v89|, s84
	v_add_f32_e32 v90, 1.0, v90
	v_add_f32_e32 v91, 1.0, v91
	v_log_f32_e32 v90, v90
	v_log_f32_e32 v91, v91
	v_exp_f32_e32 v92, v92
	v_exp_f32_e32 v93, v93
	v_min_f32_e32 v87, 0, v87
	v_min_f32_e32 v86, 0, v86
	v_pk_fma_f32 v[86:87], v[90:91], s[66:67], v[86:87] op_sel_hi:[1,0,1] neg_lo:[1,0,0] neg_hi:[1,0,0]
	v_add_f32_e32 v90, 1.0, v92
	v_add_f32_e32 v91, 1.0, v93
	v_log_f32_e32 v90, v90
	v_log_f32_e32 v91, v91
	v_min_f32_e32 v89, 0, v89
	v_min_f32_e32 v88, 0, v88
	v_pk_fma_f32 v[88:89], v[90:91], s[66:67], v[88:89] op_sel_hi:[1,0,1] neg_lo:[1,0,0] neg_hi:[1,0,0]
	v_pk_mul_f32 v[86:87], v[86:87], s[68:69] op_sel_hi:[1,0]
	v_pk_mul_f32 v[88:89], v[88:89], s[68:69] op_sel_hi:[1,0]
	s_nop 1
	v_add_f32_dpp v86, v86, v86 row_shr:1 row_mask:0xf bank_mask:0xf
	v_add_f32_dpp v87, v87, v87 row_shr:1 row_mask:0xf bank_mask:0xf
	v_add_f32_dpp v88, v88, v88 row_shr:1 row_mask:0xf bank_mask:0xf
	v_add_f32_dpp v89, v89, v89 row_shr:1 row_mask:0xf bank_mask:0xf
	v_add_f32_dpp v86, v86, v86 row_shr:2 row_mask:0xf bank_mask:0xf
	v_add_f32_dpp v87, v87, v87 row_shr:2 row_mask:0xf bank_mask:0xf
	v_add_f32_dpp v88, v88, v88 row_shr:2 row_mask:0xf bank_mask:0xf
	v_add_f32_dpp v89, v89, v89 row_shr:2 row_mask:0xf bank_mask:0xf
	v_add_f32_dpp v86, v86, v86 row_shr:4 row_mask:0xf bank_mask:0xf
	v_add_f32_dpp v87, v87, v87 row_shr:4 row_mask:0xf bank_mask:0xf
	v_add_f32_dpp v88, v88, v88 row_shr:4 row_mask:0xf bank_mask:0xf
	v_add_f32_dpp v89, v89, v89 row_shr:4 row_mask:0xf bank_mask:0xf
; __device__ __forceinline__ float logsig16(float x) { return ((x < 0.f ? x : 0.f) - 0.6931471805599453f * __builtin_amdgcn_logf(1.0f + __builtin_amdgcn_exp2f(-1.4426950408889634f * fabsf(x)))) * (1.0f / 16.0f); }
; #define MFMA16(a, b, c) __builtin_amdgcn_mfma_f32_16x16x32_bf16((a), (b), (c), 0, 0, 0)
; template <int layer> __device__ __forceinline__ void layer_phases(const Ctx& c, unsigned char* lds) {
;     ...
;                     for (int ct = 0; ct < 8; ++ct) { const f32x4 z = MFMA16(wfr[ct], afr, ((f32x4){0.f, 0.f, 0.f, 0.f})) + bcl[ct];
;                         f32x4 v; v[0] = pg8::logsig16(z[0]); v[1] = pg8::logsig16(z[1]); v[2] = pg8::logsig16(z[2]); v[3] = pg8::logsig16(z[3]);
; #pragma unroll
;                         for (int st = 1; st < 16; st <<= 1) { f32x4 t;
; #pragma unroll
;                             for (int j = 0; j < 4; ++j) t[j] = __shfl_up(v[j], st, 16);
;                             if (ql >= st) v += t; }
;                         cv[ct] = v;
;                         if (ql == 15) *(f32x4*)(tot + rt * 256 + 16 * (8 * kh + ct) + 4 * g4) = v; }
	v_add_f32_dpp v86, v86, v86 row_shr:8 row_mask:0xf bank_mask:0xf
	v_add_f32_dpp v87, v87, v87 row_shr:8 row_mask:0xf bank_mask:0xf
	v_add_f32_dpp v88, v88, v88 row_shr:8 row_mask:0xf bank_mask:0xf
	v_add_f32_dpp v89, v89, v89 row_shr:8 row_mask:0xf bank_mask:0xf
	s_and_saveexec_b64 s[16:17], s[6:7]
	v_add_u32_e32 v90, s69, v107
	ds_write_b128 v90, v[86:89] offset:8192
	s_or_b64 exec, exec, s[16:17]
	v_mfma_f32_16x16x32_bf16 v[90:93], v[38:41], v[70:73], 0
	s_nop 7
	v_pk_add_f32 v[90:91], v[46:47], v[90:91]
	v_pk_add_f32 v[92:93], v[48:49], v[92:93]
	v_mul_f32_e64 v94, |v90|, s84
	v_mul_f32_e64 v95, |v91|, s84
	v_exp_f32_e32 v94, v94
	v_exp_f32_e32 v95, v95
	v_mul_f32_e64 v96, |v92|, s84
	v_mul_f32_e64 v97, |v93|, s84
	v_add_f32_e32 v94, 1.0, v94
	v_add_f32_e32 v95, 1.0, v95
	v_log_f32_e32 v94, v94
	v_log_f32_e32 v95, v95
	v_exp_f32_e32 v96, v96
	v_exp_f32_e32 v97, v97
	v_min_f32_e32 v91, 0, v91
	v_min_f32_e32 v90, 0, v90
	v_pk_fma_f32 v[90:91], v[94:95], s[66:67], v[90:91] op_sel_hi:[1,0,1] neg_lo:[1,0,0] neg_hi:[1,0,0]
	v_add_f32_e32 v94, 1.0, v96
	v_add_f32_e32 v95, 1.0, v97
	v_log_f32_e32 v94, v94
	v_log_f32_e32 v95, v95
	v_min_f32_e32 v93, 0, v93
	v_min_f32_e32 v92, 0, v92
	v_pk_fma_f32 v[92:93], v[94:95], s[66:67], v[92:93] op_sel_hi:[1,0,1] neg_lo:[1,0,0] neg_hi:[1,0,0]
	v_pk_mul_f32 v[90:91], v[90:91], s[68:69] op_sel_hi:[1,0]
	v_pk_mul_f32 v[92:93], v[92:93], s[68:69] op_sel_hi:[1,0]
	s_nop 1
	v_add_f32_dpp v90, v90, v90 row_shr:1 row_mask:0xf bank_mask:0xf
	v_add_f32_dpp v91, v91, v91 row_shr:1 row_mask:0xf bank_mask:0xf
	v_add_f32_dpp v92, v92, v92 row_shr:1 row_mask:0xf bank_mask:0xf
	v_add_f32_dpp v93, v93, v93 row_shr:1 row_mask:0xf bank_mask:0xf
	v_add_f32_dpp v90, v90, v90 row_shr:2 row_mask:0xf bank_mask:0xf
	v_add_f32_dpp v91, v91, v91 row_shr:2 row_mask:0xf bank_mask:0xf
	v_add_f32_dpp v92, v92, v92 row_shr:2 row_mask:0xf bank_mask:0xf
	v_add_f32_dpp v93, v93, v93 row_shr:2 row_mask:0xf bank_mask:0xf
	v_add_f32_dpp v90, v90, v90 row_shr:4 row_mask:0xf bank_mask:0xf
	v_add_f32_dpp v91, v91, v91 row_shr:4 row_mask:0xf bank_mask:0xf
	v_add_f32_dpp v92, v92, v92 row_shr:4 row_mask:0xf bank_mask:0xf
	v_add_f32_dpp v93, v93, v93 row_shr:4 row_mask:0xf bank_mask:0xf
	v_add_f32_dpp v90, v90, v90 row_shr:8 row_mask:0xf bank_mask:0xf
	v_add_f32_dpp v91, v91, v91 row_shr:8 row_mask:0xf bank_mask:0xf
	v_add_f32_dpp v92, v92, v92 row_shr:8 row_mask:0xf bank_mask:0xf
	v_add_f32_dpp v93, v93, v93 row_shr:8 row_mask:0xf bank_mask:0xf
	s_and_saveexec_b64 s[16:17], s[6:7]
	v_add_u32_e32 v94, s80, v107
	ds_write_b128 v94, v[90:93] offset:8192
	s_or_b64 exec, exec, s[16:17]
	v_mfma_f32_16x16x32_bf16 v[94:97], v[50:53], v[70:73], 0
	s_nop 7
	v_pk_add_f32 v[94:95], v[58:59], v[94:95]
	v_pk_add_f32 v[96:97], v[60:61], v[96:97]
	v_mul_f32_e64 v102, |v94|, s84
	v_mul_f32_e64 v103, |v95|, s84
	v_exp_f32_e32 v102, v102
	v_exp_f32_e32 v103, v103
	v_mul_f32_e64 v104, |v96|, s84
	v_mul_f32_e64 v105, |v97|, s84
	v_add_f32_e32 v102, 1.0, v102
	v_add_f32_e32 v103, 1.0, v103
	v_log_f32_e32 v102, v102
	v_log_f32_e32 v103, v103
	v_exp_f32_e32 v104, v104
	v_exp_f32_e32 v105, v105
	v_min_f32_e32 v95, 0, v95
	v_min_f32_e32 v94, 0, v94
	v_pk_fma_f32 v[94:95], v[102:103], s[66:67], v[94:95] op_sel_hi:[1,0,1] neg_lo:[1,0,0] neg_hi:[1,0,0]
	v_add_f32_e32 v102, 1.0, v104
	v_add_f32_e32 v103, 1.0, v105
	v_log_f32_e32 v102, v102
	v_log_f32_e32 v103, v103
	v_min_f32_e32 v97, 0, v97
	v_min_f32_e32 v96, 0, v96
	v_pk_fma_f32 v[96:97], v[102:103], s[66:67], v[96:97] op_sel_hi:[1,0,1] neg_lo:[1,0,0] neg_hi:[1,0,0]
	v_pk_mul_f32 v[94:95], v[94:95], s[68:69] op_sel_hi:[1,0]
	v_pk_mul_f32 v[96:97], v[96:97], s[68:69] op_sel_hi:[1,0]
	s_nop 1
	v_add_f32_dpp v94, v94, v94 row_shr:1 row_mask:0xf bank_mask:0xf
	v_add_f32_dpp v95, v95, v95 row_shr:1 row_mask:0xf bank_mask:0xf
	v_add_f32_dpp v96, v96, v96 row_shr:1 row_mask:0xf bank_mask:0xf
	v_add_f32_dpp v97, v97, v97 row_shr:1 row_mask:0xf bank_mask:0xf
	v_add_f32_dpp v94, v94, v94 row_shr:2 row_mask:0xf bank_mask:0xf
	v_add_f32_dpp v95, v95, v95 row_shr:2 row_mask:0xf bank_mask:0xf
	v_add_f32_dpp v96, v96, v96 row_shr:2 row_mask:0xf bank_mask:0xf
	v_add_f32_dpp v97, v97, v97 row_shr:2 row_mask:0xf bank_mask:0xf
	v_add_f32_dpp v94, v94, v94 row_shr:4 row_mask:0xf bank_mask:0xf
	v_add_f32_dpp v95, v95, v95 row_shr:4 row_mask:0xf bank_mask:0xf
	v_add_f32_dpp v96, v96, v96 row_shr:4 row_mask:0xf bank_mask:0xf
	v_add_f32_dpp v97, v97, v97 row_shr:4 row_mask:0xf bank_mask:0xf
	v_add_f32_dpp v94, v94, v94 row_shr:8 row_mask:0xf bank_mask:0xf
	v_add_f32_dpp v95, v95, v95 row_shr:8 row_mask:0xf bank_mask:0xf
	v_add_f32_dpp v96, v96, v96 row_shr:8 row_mask:0xf bank_mask:0xf
	v_add_f32_dpp v97, v97, v97 row_shr:8 row_mask:0xf bank_mask:0xf
	s_and_saveexec_b64 s[16:17], s[6:7]
	v_add_u32_e32 v102, s81, v107
	ds_write_b128 v102, v[94:97] offset:8192
	s_or_b64 exec, exec, s[16:17]
	v_mfma_f32_16x16x32_bf16 v[70:73], v[54:57], v[70:73], 0
	s_nop 7
	v_pk_add_f32 v[70:71], v[62:63], v[70:71]
	v_pk_add_f32 v[72:73], v[64:65], v[72:73]
	v_mul_f32_e64 v102, |v70|, s84
	v_mul_f32_e64 v103, |v71|, s84
	v_exp_f32_e32 v102, v102
	v_exp_f32_e32 v103, v103
	v_mul_f32_e64 v104, |v72|, s84
	v_mul_f32_e64 v105, |v73|, s84
	v_add_f32_e32 v102, 1.0, v102
	v_add_f32_e32 v103, 1.0, v103
	v_log_f32_e32 v102, v102
	v_log_f32_e32 v103, v103
	v_exp_f32_e32 v104, v104
	v_exp_f32_e32 v105, v105
	v_min_f32_e32 v71, 0, v71
	v_min_f32_e32 v70, 0, v70
	v_pk_fma_f32 v[70:71], v[102:103], s[66:67], v[70:71] op_sel_hi:[1,0,1] neg_lo:[1,0,0] neg_hi:[1,0,0]
; __device__ __forceinline__ float logsig16(float x) { return ((x < 0.f ? x : 0.f) - 0.6931471805599453f * __builtin_amdgcn_logf(1.0f + __builtin_amdgcn_exp2f(-1.4426950408889634f * fabsf(x)))) * (1.0f / 16.0f); }
; #define MFMA16(a, b, c) __builtin_amdgcn_mfma_f32_16x16x32_bf16((a), (b), (c), 0, 0, 0)
; template <int layer> __device__ __forceinline__ void layer_phases(const Ctx& c, unsigned char* lds) {
;     ...
;                     for (int ct = 0; ct < 8; ++ct) { const f32x4 z = MFMA16(wfr[ct], afr, ((f32x4){0.f, 0.f, 0.f, 0.f})) + bcl[ct];
;                         f32x4 v; v[0] = pg8::logsig16(z[0]); v[1] = pg8::logsig16(z[1]); v[2] = pg8::logsig16(z[2]); v[3] = pg8::logsig16(z[3]);
; #pragma unroll
;                         for (int st = 1; st < 16; st <<= 1) { f32x4 t;
; #pragma unroll
;                             for (int j = 0; j < 4; ++j) t[j] = __shfl_up(v[j], st, 16);
;                             if (ql >= st) v += t; }
;                         cv[ct] = v;
;                         if (ql == 15) *(f32x4*)(tot + rt * 256 + 16 * (8 * kh + ct) + 4 * g4) = v; }
;                     __syncthreads();
; #pragma unroll
;                     for (int ct = 0; ct < 8; ++ct) { f32x4 v = cv[ct];
; #pragma unroll
;                         for (int r2 = 0; r2 < 3; ++r2) if (r2 < rt) v += *(const f32x4*)(tot + r2 * 256 + 16 * (8 * kh + ct) + 4 * g4);
;                         *(v4u*)(LA + (size_t)(blk * 64 + rt * 16 + (lane >> 2)) * 256 + 16 * (8 * kh + ct) + 4 * (lane & 3)) = lane_perm4(__builtin_bit_cast(v4u, v), QSRC_ST(lane)); } }
	v_add_f32_e32 v102, 1.0, v104
	v_add_f32_e32 v103, 1.0, v105
	v_log_f32_e32 v102, v102
	v_log_f32_e32 v103, v103
	v_min_f32_e32 v73, 0, v73
	v_min_f32_e32 v72, 0, v72
	v_pk_fma_f32 v[72:73], v[102:103], s[66:67], v[72:73] op_sel_hi:[1,0,1] neg_lo:[1,0,0] neg_hi:[1,0,0]
	v_pk_mul_f32 v[70:71], v[70:71], s[68:69] op_sel_hi:[1,0]
	v_pk_mul_f32 v[72:73], v[72:73], s[68:69] op_sel_hi:[1,0]
	s_nop 1
	v_add_f32_dpp v70, v70, v70 row_shr:1 row_mask:0xf bank_mask:0xf
	v_add_f32_dpp v71, v71, v71 row_shr:1 row_mask:0xf bank_mask:0xf
	v_add_f32_dpp v72, v72, v72 row_shr:1 row_mask:0xf bank_mask:0xf
	v_add_f32_dpp v73, v73, v73 row_shr:1 row_mask:0xf bank_mask:0xf
	v_add_f32_dpp v70, v70, v70 row_shr:2 row_mask:0xf bank_mask:0xf
	v_add_f32_dpp v71, v71, v71 row_shr:2 row_mask:0xf bank_mask:0xf
	v_add_f32_dpp v72, v72, v72 row_shr:2 row_mask:0xf bank_mask:0xf
	v_add_f32_dpp v73, v73, v73 row_shr:2 row_mask:0xf bank_mask:0xf
	v_add_f32_dpp v70, v70, v70 row_shr:4 row_mask:0xf bank_mask:0xf
	v_add_f32_dpp v71, v71, v71 row_shr:4 row_mask:0xf bank_mask:0xf
	v_add_f32_dpp v72, v72, v72 row_shr:4 row_mask:0xf bank_mask:0xf
	v_add_f32_dpp v73, v73, v73 row_shr:4 row_mask:0xf bank_mask:0xf
	v_add_f32_dpp v70, v70, v70 row_shr:8 row_mask:0xf bank_mask:0xf
	v_add_f32_dpp v71, v71, v71 row_shr:8 row_mask:0xf bank_mask:0xf
	v_add_f32_dpp v72, v72, v72 row_shr:8 row_mask:0xf bank_mask:0xf
	v_add_f32_dpp v73, v73, v73 row_shr:8 row_mask:0xf bank_mask:0xf
	s_and_saveexec_b64 s[16:17], s[6:7]
	v_add_u32_e32 v98, s82, v107
	ds_write_b128 v98, v[70:73] offset:8192
	s_or_b64 exec, exec, s[16:17]
	v_cndmask_b32_e64 v98, 0, 1, s[58:59]
	v_cmp_ne_u32_e64 s[16:17], 1, v98
	s_andn2_b64 vcc, exec, s[58:59]
	v_add_u32_e32 v98, s3, v144
	s_waitcnt lgkmcnt(0)
	s_barrier
	v_add_u32_e32 v250, s3, v144
	ds_read_b128 v[150:153], v250 offset:8192
	ds_read_b128 v[154:157], v250 offset:9216
	ds_read_b128 v[158:161], v250 offset:10240
	v_add_u32_e32 v251, s56, v144
	ds_read_b128 v[162:165], v251 offset:8192
	ds_read_b128 v[166:169], v251 offset:9216
	ds_read_b128 v[170:173], v251 offset:10240
	v_add_u32_e32 v250, s57, v144
	ds_read_b128 v[174:177], v250 offset:8192
	ds_read_b128 v[178:181], v250 offset:9216
	ds_read_b128 v[182:185], v250 offset:10240
	v_add_u32_e32 v251, s67, v144
	ds_read_b128 v[186:189], v251 offset:8192
	ds_read_b128 v[190:193], v251 offset:9216
	ds_read_b128 v[194:197], v251 offset:10240
	v_add_u32_e32 v250, s69, v144
	ds_read_b128 v[198:201], v250 offset:8192
	ds_read_b128 v[202:205], v250 offset:9216
	ds_read_b128 v[206:209], v250 offset:10240
	v_add_u32_e32 v251, s80, v144
	ds_read_b128 v[210:213], v251 offset:8192
	ds_read_b128 v[214:217], v251 offset:9216
	ds_read_b128 v[218:221], v251 offset:10240
	v_add_u32_e32 v250, s81, v144
	ds_read_b128 v[222:225], v250 offset:8192
	ds_read_b128 v[230:233], v250 offset:9216
	ds_read_b128 v[234:237], v250 offset:10240
	v_add_u32_e32 v251, s82, v144
	ds_read_b128 v[238:241], v251 offset:8192
	ds_read_b128 v[242:245], v251 offset:9216
	ds_read_b128 v[246:249], v251 offset:10240
	s_waitcnt lgkmcnt(0)
	s_andn2_b64 vcc, exec, s[58:59]
	s_cbranch_vccnz .Lla_skip1_0
	v_pk_add_f32 v[68:69], v[68:69], v[152:153]
	v_pk_add_f32 v[66:67], v[66:67], v[150:151]
	v_pk_add_f32 v[76:77], v[76:77], v[164:165]
	v_pk_add_f32 v[74:75], v[74:75], v[162:163]
	v_pk_add_f32 v[80:81], v[80:81], v[176:177]
	v_pk_add_f32 v[78:79], v[78:79], v[174:175]
	v_pk_add_f32 v[84:85], v[84:85], v[188:189]
	v_pk_add_f32 v[82:83], v[82:83], v[186:187]
	v_pk_add_f32 v[88:89], v[88:89], v[200:201]
	v_pk_add_f32 v[86:87], v[86:87], v[198:199]
	v_pk_add_f32 v[92:93], v[92:93], v[212:213]
	v_pk_add_f32 v[90:91], v[90:91], v[210:211]
	v_pk_add_f32 v[96:97], v[96:97], v[224:225]
	v_pk_add_f32 v[94:95], v[94:95], v[222:223]
	v_pk_add_f32 v[72:73], v[72:73], v[240:241]
	v_pk_add_f32 v[70:71], v[70:71], v[238:239]
.Lla_skip1_0:
	s_andn2_b64 vcc, exec, s[60:61]
	s_cbranch_vccnz .Lla_skip1_1
	v_pk_add_f32 v[68:69], v[68:69], v[156:157]
	v_pk_add_f32 v[66:67], v[66:67], v[154:155]
	v_pk_add_f32 v[76:77], v[76:77], v[168:169]
	v_pk_add_f32 v[74:75], v[74:75], v[166:167]
	v_pk_add_f32 v[80:81], v[80:81], v[180:181]
	v_pk_add_f32 v[78:79], v[78:79], v[178:179]
	v_pk_add_f32 v[84:85], v[84:85], v[192:193]
	v_pk_add_f32 v[82:83], v[82:83], v[190:191]
	v_pk_add_f32 v[88:89], v[88:89], v[204:205]
	v_pk_add_f32 v[86:87], v[86:87], v[202:203]
	v_pk_add_f32 v[92:93], v[92:93], v[216:217]
	v_pk_add_f32 v[90:91], v[90:91], v[214:215]
	v_pk_add_f32 v[96:97], v[96:97], v[232:233]
	v_pk_add_f32 v[94:95], v[94:95], v[230:231]
	v_pk_add_f32 v[72:73], v[72:73], v[244:245]
	v_pk_add_f32 v[70:71], v[70:71], v[242:243]
.Lla_skip1_1:
	s_andn2_b64 vcc, exec, s[62:63]
	s_cbranch_vccnz .Lla_skip1_2
	v_pk_add_f32 v[68:69], v[68:69], v[160:161]
	v_pk_add_f32 v[66:67], v[66:67], v[158:159]
	v_pk_add_f32 v[76:77], v[76:77], v[172:173]
	v_pk_add_f32 v[74:75], v[74:75], v[170:171]
	v_pk_add_f32 v[80:81], v[80:81], v[184:185]
	v_pk_add_f32 v[78:79], v[78:79], v[182:183]
	v_pk_add_f32 v[84:85], v[84:85], v[196:197]
	v_pk_add_f32 v[82:83], v[82:83], v[194:195]
	v_pk_add_f32 v[88:89], v[88:89], v[208:209]
	v_pk_add_f32 v[86:87], v[86:87], v[206:207]
	v_pk_add_f32 v[92:93], v[92:93], v[220:221]
	v_pk_add_f32 v[90:91], v[90:91], v[218:219]
	v_pk_add_f32 v[96:97], v[96:97], v[236:237]
	v_pk_add_f32 v[94:95], v[94:95], v[234:235]
	v_pk_add_f32 v[72:73], v[72:73], v[248:249]
	v_pk_add_f32 v[70:71], v[70:71], v[246:247]
